# P9: non-temporal hint on the row loads on top of the write-through output stores
# baseline (speedup 1.0000x reference)
.LBB0_1205:
	s_add_i32 s1, s9, -3
	s_add_i32 s2, s9, -2
	s_add_i32 s3, s9, -1
	v_readlane_b32 s0, v130, s9
	v_readlane_b32 s24, v130, s1
	v_readlane_b32 s2, v130, s2
	v_readlane_b32 s26, v130, s3
	v_lshl_add_u64 v[0:1], s[92:93], 0, v[106:107]
	s_ashr_i32 s1, s0, 31
	s_ashr_i32 s25, s24, 31
	s_ashr_i32 s3, s2, 31
	s_ashr_i32 s27, s26, 31
	v_add_co_u32_e32 v0, vcc, s11, v0
	s_add_u32 s28, s92, s21
	v_mov_b32_e32 v6, 0
	v_addc_co_u32_e32 v1, vcc, 0, v1, vcc
	s_addc_u32 s29, s93, s22
	s_lshl_b64 s[24:25], s[24:25], 11
	v_lshl_add_u64 v[2:3], s[92:93], 0, v[110:111]
	v_lshl_add_u64 v[4:5], s[92:93], 0, v[108:109]
	s_lshl_b64 s[2:3], s[2:3], 11
	s_lshl_b64 s[26:27], s[26:27], 11
	s_lshl_b64 s[0:1], s[0:1], 11
	global_load_dwordx2 v[212:213], v126, s[28:29]
	global_load_dwordx4 v[132:135], v[0:1], off nt
	global_load_dwordx4 v[136:139], v[2:3], off nt
	global_load_dwordx4 v[140:143], v[0:1], off offset:2048 nt
	global_load_dwordx4 v[144:147], v[4:5], off nt
	v_lshl_add_u64 v[0:1], v[112:113], 0, s[24:25]
	v_lshl_add_u64 v[2:3], v[112:113], 0, s[2:3]
	v_lshl_add_u64 v[4:5], v[112:113], 0, s[26:27]
	v_lshl_add_u64 v[8:9], v[112:113], 0, s[0:1]
	global_load_dwordx4 v[92:95], v[0:1], off nt
	global_load_dwordx4 v[88:91], v[2:3], off nt
	global_load_dwordx4 v[84:87], v[4:5], off nt
	global_load_dwordx4 v[80:83], v[8:9], off nt
	global_load_dwordx4 v[76:79], v[0:1], off offset:1024 nt
	global_load_dwordx4 v[72:75], v[2:3], off offset:1024 nt
	global_load_dwordx4 v[68:71], v[4:5], off offset:1024 nt
	global_load_dwordx4 v[64:67], v[8:9], off offset:1024 nt
	v_lshl_add_u32 v44, v6, 2, v129
	ds_read_b128 v[148:151], v44
	ds_read_b128 v[152:155], v44 offset:1024
	ds_read_b128 v[156:159], v44 offset:8192
	ds_read_b128 v[160:163], v44 offset:9216
	ds_read_b128 v[164:167], v44 offset:2048
	ds_read_b128 v[168:171], v44 offset:3072
	ds_read_b128 v[172:175], v44 offset:10240
	ds_read_b128 v[176:179], v44 offset:11264
	ds_read_b128 v[180:183], v44 offset:4096
	ds_read_b128 v[184:187], v44 offset:5120
	ds_read_b128 v[188:191], v44 offset:12288
	ds_read_b128 v[192:195], v44 offset:13312
	ds_read_b128 v[196:199], v44 offset:6144
	ds_read_b128 v[200:203], v44 offset:7168
	ds_read_b128 v[204:207], v44 offset:14336
	ds_read_b128 v[208:211], v44 offset:15360
	ds_read_b128 v[16:19], v44 offset:16384
	ds_read_b128 v[0:3], v44 offset:17408
	ds_read_b128 v[48:51], v44 offset:24576
	ds_read_b128 v[32:35], v44 offset:25600
	ds_read_b128 v[20:23], v44 offset:18432
	ds_read_b128 v[4:7], v44 offset:19456
	ds_read_b128 v[52:55], v44 offset:26624
	ds_read_b128 v[36:39], v44 offset:27648
	ds_read_b128 v[24:27], v44 offset:20480
	ds_read_b128 v[8:11], v44 offset:21504
	ds_read_b128 v[56:59], v44 offset:28672
	ds_read_b128 v[40:43], v44 offset:29696
	ds_read_b128 v[28:31], v44 offset:22528
	ds_read_b128 v[12:15], v44 offset:23552
	ds_read_b128 v[60:63], v44 offset:30720
	ds_read_b128 v[44:47], v44 offset:31744
	s_add_u32 s4, s4, s6
	s_addc_u32 s5, s5, s7
	s_add_i32 s9, s9, 4
	s_add_u32 s21, s21, s12
	s_addc_u32 s22, s22, s13
	v_lshl_add_u64 v[116:117], s[16:17], 0, v[96:97]
	v_lshl_add_u64 v[118:119], s[16:17], 0, v[98:99]
	v_lshl_add_u64 v[120:121], s[16:17], 0, v[100:101]
	v_lshl_add_u64 v[122:123], s[16:17], 0, v[102:103]
	v_lshl_add_u64 v[124:125], s[16:17], 0, v[104:105]
	v_cmp_lt_u64_e32 vcc, s[4:5], v[114:115]
	s_add_u32 s16, s16, s18
	s_addc_u32 s17, s17, s19
	s_and_b64 s[0:1], exec, vcc
	v_lshl_add_u64 v[108:109], v[108:109], 0, s[14:15]
	v_lshl_add_u64 v[106:107], v[106:107], 0, s[14:15]
	v_lshl_add_u64 v[110:111], v[110:111], 0, s[14:15]
	s_waitcnt vmcnt(11)
	v_mov_b32_e32 v131, v134
	v_mov_b32_e32 v134, v135
	s_nop 0
	v_permlane16_swap_b32_e32 v132, v131
	s_waitcnt vmcnt(10)
	v_mov_b32_e32 v135, v138
	v_permlane16_swap_b32_e32 v133, v134
	s_waitcnt vmcnt(7)
	v_mov_b32_e32 v230, v93
	s_waitcnt vmcnt(2)
	v_mov_b32_e32 v235, v73
	s_waitcnt vmcnt(1)
	v_mov_b32_e32 v236, v69
	s_waitcnt vmcnt(0)
	v_mov_b32_e32 v237, v67
	v_lshlrev_b32_e32 v67, 16, v132
	v_and_b32_e32 v69, 0xffff0000, v132
	v_mov_b32_e32 v138, v139
	v_mov_b32_e32 v139, v142
	v_mov_b32_e32 v142, v143
	v_mov_b32_e32 v143, v146
	v_mov_b32_e32 v146, v147
	v_permlane16_swap_b32_e32 v136, v135
	v_mov_b32_e32 v231, v89
	v_mov_b32_e32 v234, v79
	v_lshlrev_b32_e32 v73, 16, v133
	v_and_b32_e32 v79, 0xffff0000, v133
	v_permlane16_swap_b32_e32 v92, v230
	v_permlane16_swap_b32_e32 v94, v95
	v_permlane16_swap_b32_e32 v72, v235
	v_sub_f32_e32 v133, v69, v212
	v_sub_f32_e32 v132, v67, v212
	v_permlane16_swap_b32_e32 v137, v138
	v_permlane16_swap_b32_e32 v140, v139
	v_permlane16_swap_b32_e32 v141, v142
	v_permlane16_swap_b32_e32 v144, v143
	v_permlane16_swap_b32_e32 v145, v146
	v_lshlrev_b32_e32 v89, 16, v134
	v_and_b32_e32 v93, 0xffff0000, v134
	v_lshlrev_b32_e32 v216, 16, v135
	v_and_b32_e32 v217, 0xffff0000, v135
	v_permlane16_swap_b32_e32 v88, v231
	v_permlane16_swap_b32_e32 v90, v91
	v_permlane16_swap_b32_e32 v68, v236
	v_permlane16_swap_b32_e32 v66, v237
	v_sub_f32_e32 v135, v79, v212
	v_sub_f32_e32 v134, v73, v212
	v_permlane32_swap_b32_e32 v230, v95
	v_mov_b32_e32 v250, v72
	v_pk_mul_f32 v[72:73], v[212:213], v[132:133] op_sel:[1,0]
	v_mov_b32_e32 v232, v87
	v_mov_b32_e32 v233, v83
	v_lshlrev_b32_e32 v83, 16, v131
	v_and_b32_e32 v87, 0xffff0000, v131
	v_lshlrev_b32_e32 v131, 16, v136
	v_and_b32_e32 v147, 0xffff0000, v136
	v_lshlrev_b32_e32 v214, 16, v137
	v_and_b32_e32 v215, 0xffff0000, v137
	v_lshlrev_b32_e32 v218, 16, v138
	v_and_b32_e32 v219, 0xffff0000, v138
	v_lshlrev_b32_e32 v220, 16, v140
	v_and_b32_e32 v221, 0xffff0000, v140
	v_lshlrev_b32_e32 v222, 16, v141
	v_and_b32_e32 v223, 0xffff0000, v141
	v_lshlrev_b32_e32 v224, 16, v139
	v_and_b32_e32 v225, 0xffff0000, v139
	v_lshlrev_b32_e32 v228, 16, v144
	v_and_b32_e32 v229, 0xffff0000, v144
	v_lshlrev_b32_e32 v238, 16, v145
	v_and_b32_e32 v239, 0xffff0000, v145
	v_lshlrev_b32_e32 v240, 16, v143
	v_and_b32_e32 v241, 0xffff0000, v143
	v_permlane32_swap_b32_e32 v231, v91
	v_mov_b32_e32 v251, v68
	v_pk_mul_f32 v[68:69], v[212:213], v[134:135] op_sel:[1,0]
	v_mov_b32_e32 v252, v66
	s_waitcnt lgkmcnt(14)
	v_pk_fma_f32 v[66:67], v[72:73], v[148:149], v[156:157]
	v_cvt_pk_f32_fp8_e32 v[72:73], v230
	v_lshlrev_b32_e32 v226, 16, v142
	v_and_b32_e32 v227, 0xffff0000, v142
	v_lshlrev_b32_e32 v242, 16, v146
	v_and_b32_e32 v243, 0xffff0000, v146
	v_permlane16_swap_b32_e32 v86, v232
	v_permlane16_swap_b32_e32 v82, v233
	v_permlane16_swap_b32_e32 v76, v77
	v_permlane16_swap_b32_e32 v78, v234
	v_sub_f32_e32 v137, v87, v212
	v_sub_f32_e32 v136, v83, v212
	v_sub_f32_e32 v141, v215, v212
	v_sub_f32_e32 v140, v214, v212
	v_sub_f32_e32 v143, v147, v212
	v_sub_f32_e32 v142, v131, v212
	v_sub_f32_e32 v145, v219, v212
	v_sub_f32_e32 v144, v218, v212
	v_sub_f32_e32 v147, v217, v212
	v_sub_f32_e32 v146, v216, v212
	v_sub_f32_e32 v215, v221, v212
	v_sub_f32_e32 v214, v220, v212
	v_sub_f32_e32 v217, v223, v212
	v_sub_f32_e32 v216, v222, v212
	v_sub_f32_e32 v219, v225, v212
	v_sub_f32_e32 v218, v224, v212
	v_sub_f32_e32 v223, v239, v212
	v_sub_f32_e32 v222, v238, v212
	v_sub_f32_e32 v225, v229, v212
	v_sub_f32_e32 v224, v228, v212
	v_sub_f32_e32 v229, v241, v212
	v_sub_f32_e32 v228, v240, v212
	v_mov_b32_e32 v131, v92
	v_pk_fma_f32 v[68:69], v[68:69], v[150:151], v[158:159]
	v_cvt_pk_f32_fp8_sdwa v[148:149], v230 src0_sel:WORD_1
	v_cvt_pk_f32_fp8_e32 v[158:159], v231
	v_permlane16_swap_b32_e32 v84, v85
	v_permlane16_swap_b32_e32 v80, v81
	v_permlane16_swap_b32_e32 v74, v75
	v_permlane16_swap_b32_e32 v70, v71
	v_permlane16_swap_b32_e32 v64, v65
	v_sub_f32_e32 v139, v93, v212
	v_sub_f32_e32 v138, v89, v212
	v_sub_f32_e32 v221, v227, v212
	v_sub_f32_e32 v220, v226, v212
	v_sub_f32_e32 v227, v243, v212
	v_sub_f32_e32 v226, v242, v212
	v_mov_b32_e32 v238, v88
	v_mov_b32_e32 v239, v86
	v_mov_b32_e32 v240, v82
	v_mov_b32_e32 v241, v78
	v_permlane32_swap_b32_e32 v77, v234
	v_pk_mul_f32 v[82:83], v[212:213], v[136:137] op_sel:[1,0]
	v_pk_mul_f32 v[92:93], v[212:213], v[146:147] op_sel:[1,0]
	v_pk_mul_f32 v[132:133], v[212:213], v[144:145] op_sel:[1,0]
	v_pk_mul_f32 v[136:137], v[212:213], v[214:215] op_sel:[1,0]
	v_pk_mul_f32 v[144:145], v[212:213], v[222:223] op_sel:[1,0]
	v_pk_mul_f32 v[146:147], v[212:213], v[228:229] op_sel:[1,0]
	v_permlane32_swap_b32_e32 v131, v94
	v_cvt_pk_f32_fp8_sdwa v[214:215], v231 src0_sel:WORD_1
	v_permlane32_swap_b32_e32 v85, v232
	v_permlane32_swap_b32_e32 v81, v233
	v_permlane32_swap_b32_e32 v235, v75
	v_permlane32_swap_b32_e32 v236, v71
	v_pk_mul_f32 v[78:79], v[212:213], v[138:139] op_sel:[1,0]
	v_pk_mul_f32 v[86:87], v[212:213], v[142:143] op_sel:[1,0]
	v_pk_mul_f32 v[88:89], v[212:213], v[140:141] op_sel:[1,0]
	v_pk_mul_f32 v[134:135], v[212:213], v[216:217] op_sel:[1,0]
	v_pk_mul_f32 v[138:139], v[212:213], v[220:221] op_sel:[1,0]
	v_pk_mul_f32 v[140:141], v[212:213], v[218:219] op_sel:[1,0]
	v_pk_mul_f32 v[142:143], v[212:213], v[224:225] op_sel:[1,0]
	v_pk_mul_f32 v[212:213], v[212:213], v[226:227] op_sel:[1,0]
	v_permlane32_swap_b32_e32 v65, v237
	v_cvt_pk_f32_fp8_e32 v[150:151], v95
	v_cvt_pk_f32_fp8_sdwa v[156:157], v95 src0_sel:WORD_1
	v_permlane32_swap_b32_e32 v238, v90
	v_permlane32_swap_b32_e32 v84, v239
	v_permlane32_swap_b32_e32 v80, v240
	v_permlane32_swap_b32_e32 v76, v241
	v_pk_fma_f32 v[132:133], v[132:133], v[170:171], v[178:179]
	v_pk_fma_f32 v[92:93], v[92:93], v[168:169], v[176:177]
	v_cvt_pk_f32_fp8_e32 v[168:169], v77
	v_cvt_pk_f32_fp8_sdwa v[170:171], v77 src0_sel:WORD_1
	v_cvt_pk_f32_fp8_e32 v[176:177], v234
	v_cvt_pk_f32_fp8_sdwa v[178:179], v234 src0_sel:WORD_1
	v_pk_fma_f32 v[144:145], v[144:145], v[198:199], v[206:207]
	v_pk_fma_f32 v[146:147], v[146:147], v[200:201], v[208:209]
	v_cvt_pk_f32_fp8_e32 v[198:199], v131
	v_cvt_pk_f32_fp8_sdwa v[200:201], v131 src0_sel:WORD_1
	v_pk_fma_f32 v[82:83], v[82:83], v[152:153], v[160:161]
	v_pk_fma_f32 v[78:79], v[78:79], v[154:155], v[162:163]
	v_cvt_pk_f32_fp8_e32 v[152:153], v91
	v_cvt_pk_f32_fp8_sdwa v[154:155], v91 src0_sel:WORD_1
	v_cvt_pk_f32_fp8_e32 v[216:217], v232
	v_pk_fma_f32 v[88:89], v[88:89], v[166:167], v[174:175]
	v_pk_fma_f32 v[86:87], v[86:87], v[164:165], v[172:173]
	v_cvt_pk_f32_fp8_sdwa v[164:165], v232 src0_sel:WORD_1
	v_cvt_pk_f32_fp8_e32 v[174:175], v233
	v_cvt_pk_f32_fp8_sdwa v[218:219], v233 src0_sel:WORD_1
	v_permlane32_swap_b32_e32 v250, v74
	v_cvt_pk_f32_fp8_e32 v[220:221], v235
	v_cvt_pk_f32_fp8_sdwa v[222:223], v235 src0_sel:WORD_1
	v_pk_fma_f32 v[136:137], v[136:137], v[180:181], v[188:189]
	v_pk_fma_f32 v[134:135], v[134:135], v[182:183], v[190:191]
	v_cvt_pk_f32_fp8_e32 v[180:181], v75
	v_cvt_pk_f32_fp8_sdwa v[182:183], v75 src0_sel:WORD_1
	v_cvt_pk_f32_fp8_e32 v[188:189], v236
	v_cvt_pk_f32_fp8_sdwa v[190:191], v236 src0_sel:WORD_1
	v_pk_fma_f32 v[138:139], v[138:139], v[186:187], v[194:195]
	v_cvt_pk_f32_fp8_e32 v[194:195], v237
	v_cvt_pk_f32_fp8_sdwa v[226:227], v237 src0_sel:WORD_1
	v_pk_fma_f32 v[142:143], v[142:143], v[196:197], v[204:205]
	v_pk_fma_f32 v[196:197], v[212:213], v[202:203], v[210:211]
	v_cvt_pk_f32_fp8_e32 v[202:203], v94
	v_cvt_pk_f32_fp8_sdwa v[94:95], v94 src0_sel:WORD_1
	v_cvt_pk_f32_fp8_e32 v[204:205], v238
	v_cvt_pk_f32_fp8_sdwa v[206:207], v238 src0_sel:WORD_1
	v_cvt_pk_f32_fp8_e32 v[212:213], v239
	v_cvt_pk_f32_fp8_sdwa v[228:229], v239 src0_sel:WORD_1
	v_cvt_pk_f32_fp8_e32 v[232:233], v240
	v_cvt_pk_f32_fp8_sdwa v[234:235], v240 src0_sel:WORD_1
	v_cvt_pk_f32_fp8_e32 v[236:237], v76
	v_cvt_pk_f32_fp8_sdwa v[76:77], v76 src0_sel:WORD_1
	v_cvt_pk_f32_fp8_e32 v[238:239], v241
	v_cvt_pk_f32_fp8_sdwa v[240:241], v241 src0_sel:WORD_1
	v_pk_add_f32 v[72:73], v[72:73], 0 op_sel_hi:[1,0]
	v_cvt_pk_f32_fp8_e32 v[160:161], v85
	v_cvt_pk_f32_fp8_sdwa v[162:163], v85 src0_sel:WORD_1
	v_permlane32_swap_b32_e32 v251, v70
	v_cvt_pk_f32_fp8_e32 v[224:225], v71
	v_pk_fma_f32 v[140:141], v[140:141], v[184:185], v[192:193]
	v_cvt_pk_f32_fp8_sdwa v[184:185], v71 src0_sel:WORD_1
	v_cvt_pk_f32_fp8_e32 v[208:209], v90
	v_cvt_pk_f32_fp8_sdwa v[90:91], v90 src0_sel:WORD_1
	v_cvt_pk_f32_fp8_e32 v[210:211], v84
	v_cvt_pk_f32_fp8_sdwa v[84:85], v84 src0_sel:WORD_1
	v_cvt_pk_f32_fp8_e32 v[242:243], v74
	v_cvt_pk_f32_fp8_sdwa v[74:75], v74 src0_sel:WORD_1
	v_cvt_pk_f32_fp8_e32 v[248:249], v250
	v_pk_add_f32 v[72:73], v[72:73], v[158:159]
	v_cvt_pk_f32_fp8_sdwa v[158:159], v250 src0_sel:WORD_1
	v_pk_add_f32 v[148:149], v[148:149], 0 op_sel_hi:[1,0]
	v_cvt_pk_f32_fp8_e32 v[166:167], v81
	v_cvt_pk_f32_fp8_sdwa v[172:173], v81 src0_sel:WORD_1
	v_permlane32_swap_b32_e32 v64, v252
	v_cvt_pk_f32_fp8_e32 v[186:187], v65
	v_cvt_pk_f32_fp8_sdwa v[192:193], v65 src0_sel:WORD_1
	v_cvt_pk_f32_fp8_e32 v[230:231], v80
	v_cvt_pk_f32_fp8_sdwa v[80:81], v80 src0_sel:WORD_1
	v_cvt_pk_f32_fp8_e32 v[244:245], v70
	v_cvt_pk_f32_fp8_sdwa v[70:71], v70 src0_sel:WORD_1
	v_pk_add_f32 v[148:149], v[148:149], v[214:215]
	v_cvt_pk_f32_fp8_e32 v[214:215], v251
	v_cvt_pk_f32_fp8_sdwa v[250:251], v251 src0_sel:WORD_1
	v_cvt_pk_f32_fp8_e32 v[246:247], v64
	v_cvt_pk_f32_fp8_sdwa v[64:65], v64 src0_sel:WORD_1
	v_pk_add_f32 v[150:151], v[150:151], 0 op_sel_hi:[1,0]
	v_pk_add_f32 v[156:157], v[156:157], 0 op_sel_hi:[1,0]
	v_pk_add_f32 v[168:169], v[168:169], 0 op_sel_hi:[1,0]
	v_pk_add_f32 v[170:171], v[170:171], 0 op_sel_hi:[1,0]
	v_pk_add_f32 v[176:177], v[176:177], 0 op_sel_hi:[1,0]
	v_pk_add_f32 v[178:179], v[178:179], 0 op_sel_hi:[1,0]
	v_pk_add_f32 v[198:199], v[198:199], 0 op_sel_hi:[1,0]
	v_pk_add_f32 v[200:201], v[200:201], 0 op_sel_hi:[1,0]
	v_pk_add_f32 v[150:151], v[150:151], v[152:153]
	v_pk_add_f32 v[154:155], v[156:157], v[154:155]
	v_pk_add_f32 v[202:203], v[202:203], 0 op_sel_hi:[1,0]
	v_pk_add_f32 v[94:95], v[94:95], 0 op_sel_hi:[1,0]
	v_pk_add_f32 v[236:237], v[236:237], 0 op_sel_hi:[1,0]
	v_pk_add_f32 v[76:77], v[76:77], 0 op_sel_hi:[1,0]
	v_pk_add_f32 v[240:241], v[240:241], 0 op_sel_hi:[1,0]
	v_pk_add_f32 v[168:169], v[168:169], v[220:221]
	v_pk_add_f32 v[170:171], v[170:171], v[222:223]
	v_pk_add_f32 v[176:177], v[176:177], v[180:181]
	v_pk_add_f32 v[178:179], v[178:179], v[182:183]
	v_pk_add_f32 v[180:181], v[198:199], v[204:205]
	v_pk_add_f32 v[182:183], v[200:201], v[206:207]
	v_pk_add_f32 v[198:199], v[202:203], v[208:209]
	v_pk_add_f32 v[90:91], v[94:95], v[90:91]
	v_pk_add_f32 v[72:73], v[72:73], v[160:161]
	v_pk_add_f32 v[94:95], v[148:149], v[162:163]
	v_pk_add_f32 v[148:149], v[150:151], v[216:217]
	v_pk_add_f32 v[150:151], v[154:155], v[164:165]
	v_pk_add_f32 v[154:155], v[236:237], v[248:249]
	v_pk_add_f32 v[76:77], v[76:77], v[158:159]
	v_pk_add_f32 v[74:75], v[240:241], v[74:75]
	v_pk_add_f32 v[160:161], v[168:169], v[188:189]
	v_pk_add_f32 v[162:163], v[170:171], v[190:191]
	v_pk_add_f32 v[164:165], v[176:177], v[224:225]
	v_pk_add_f32 v[168:169], v[178:179], v[184:185]
	v_pk_add_f32 v[170:171], v[180:181], v[210:211]
	v_pk_add_f32 v[84:85], v[182:183], v[84:85]
	v_pk_mul_f32 v[68:69], v[68:69], s[8:9] op_sel_hi:[1,0]
	v_pk_mul_f32 v[66:67], v[66:67], s[8:9] op_sel_hi:[1,0]
	v_pk_mul_f32 v[78:79], v[78:79], s[8:9] op_sel_hi:[1,0]
	v_pk_mul_f32 v[82:83], v[82:83], s[8:9] op_sel_hi:[1,0]
	v_pk_mul_f32 v[132:133], v[132:133], s[8:9] op_sel_hi:[1,0]
	v_pk_mul_f32 v[92:93], v[92:93], s[8:9] op_sel_hi:[1,0]
	v_pk_mul_f32 v[138:139], v[138:139], s[8:9] op_sel_hi:[1,0]
	v_pk_mul_f32 v[140:141], v[140:141], s[8:9] op_sel_hi:[1,0]
	v_pk_mul_f32 v[196:197], v[196:197], s[8:9] op_sel_hi:[1,0]
	v_pk_mul_f32 v[146:147], v[146:147], s[8:9] op_sel_hi:[1,0]
	v_pk_add_f32 v[176:177], v[198:199], v[212:213]
	v_pk_add_f32 v[72:73], v[72:73], v[166:167]
	v_pk_add_f32 v[94:95], v[94:95], v[172:173]
	v_pk_add_f32 v[148:149], v[148:149], v[174:175]
	v_pk_add_f32 v[150:151], v[150:151], v[218:219]
	v_pk_add_f32 v[154:155], v[154:155], v[214:215]
	v_pk_add_f32 v[76:77], v[76:77], v[250:251]
	v_pk_add_f32 v[70:71], v[74:75], v[70:71]
	v_pk_add_f32 v[74:75], v[160:161], v[186:187]
	v_pk_add_f32 v[160:161], v[162:163], v[192:193]
	v_pk_add_f32 v[162:163], v[164:165], v[194:195]
	v_pk_add_f32 v[164:165], v[168:169], v[226:227]
	v_pk_add_f32 v[166:167], v[170:171], v[230:231]
	v_pk_add_f32 v[80:81], v[84:85], v[80:81]
	v_cvt_pk_f32_fp8_e32 v[152:153], v252
	v_pk_mul_f32 v[86:87], v[86:87], s[8:9] op_sel_hi:[1,0]
	v_pk_mul_f32 v[134:135], v[134:135], s[8:9] op_sel_hi:[1,0]
	v_pk_mul_f32 v[136:137], v[136:137], s[8:9] op_sel_hi:[1,0]
	v_pk_add_f32 v[90:91], v[90:91], v[228:229]
	v_pk_add_f32 v[84:85], v[176:177], v[232:233]
	v_pk_fma_f32 v[72:73], v[72:73], s[10:11], v[82:83] op_sel_hi:[1,0,1]
	v_pk_fma_f32 v[78:79], v[94:95], s[10:11], v[78:79] op_sel_hi:[1,0,1]
	v_pk_fma_f32 v[82:83], v[148:149], s[10:11], v[92:93] op_sel_hi:[1,0,1]
	v_pk_fma_f32 v[92:93], v[150:151], s[10:11], v[132:133] op_sel_hi:[1,0,1]
	v_pk_add_f32 v[94:95], v[154:155], v[246:247]
	v_pk_add_f32 v[64:65], v[76:77], v[64:65]
	v_pk_fma_f32 v[74:75], v[74:75], s[10:11], v[140:141] op_sel_hi:[1,0,1]
	v_pk_fma_f32 v[132:133], v[160:161], s[10:11], v[138:139] op_sel_hi:[1,0,1]
	v_pk_fma_f32 v[138:139], v[162:163], s[10:11], v[146:147] op_sel_hi:[1,0,1]
	v_pk_fma_f32 v[140:141], v[164:165], s[10:11], v[196:197] op_sel_hi:[1,0,1]
	v_pk_fma_f32 v[66:67], v[166:167], s[10:11], v[66:67] op_sel_hi:[1,0,1]
	v_pk_fma_f32 v[68:69], v[80:81], s[10:11], v[68:69] op_sel_hi:[1,0,1]
	v_cvt_pk_f32_fp8_sdwa v[156:157], v252 src0_sel:WORD_1
	v_pk_mul_f32 v[88:89], v[88:89], s[8:9] op_sel_hi:[1,0]
	v_pk_add_f32 v[238:239], v[238:239], 0 op_sel_hi:[1,0]
	v_pk_add_f32 v[90:91], v[90:91], v[234:235]
	v_pk_fma_f32 v[80:81], v[84:85], s[10:11], v[86:87] op_sel_hi:[1,0,1]
	v_pk_fma_f32 v[86:87], v[94:95], s[10:11], v[136:137] op_sel_hi:[1,0,1]
	v_pk_fma_f32 v[64:65], v[64:65], s[10:11], v[134:135] op_sel_hi:[1,0,1]
	v_add_f32_e32 v131, v140, v141
	v_add_f32_e32 v134, v138, v139
	v_add_f32_e32 v135, v68, v69
	v_add_f32_e32 v136, v66, v67
	v_pk_add_f32 v[158:159], v[238:239], v[242:243]
	v_pk_fma_f32 v[84:85], v[90:91], s[10:11], v[88:89] op_sel_hi:[1,0,1]
	v_add_f32_e32 v88, v78, v79
	v_add_f32_e32 v89, v72, v73
	v_add_f32_e32 v131, v134, v131
	v_add_f32_e32 v134, v136, v135
	v_pk_add_f32 v[158:159], v[158:159], v[244:245]
	v_add_f32_e32 v88, v89, v88
	v_add_f32_e32 v89, v84, v85
	v_add_f32_e32 v137, v80, v81
	v_add_f32_e32 v134, 0, v134
	v_pk_mul_f32 v[142:143], v[142:143], s[8:9] op_sel_hi:[1,0]
	v_pk_add_f32 v[76:77], v[158:159], v[152:153]
	v_add_f32_e32 v90, v92, v93
	v_add_f32_e32 v91, v82, v83
	v_add_f32_e32 v89, v137, v89
	v_add_f32_e32 v88, v134, v88
	v_pk_mul_f32 v[144:145], v[144:145], s[8:9] op_sel_hi:[1,0]
	v_pk_add_f32 v[70:71], v[70:71], v[156:157]
	v_pk_fma_f32 v[76:77], v[76:77], s[10:11], v[142:143] op_sel_hi:[1,0,1]
	v_add_f32_e32 v90, v91, v90
	v_add_f32_e32 v91, v64, v65
	v_add_f32_e32 v142, v86, v87
	v_add_f32_e32 v88, v88, v89
	v_pk_fma_f32 v[70:71], v[70:71], s[10:11], v[144:145] op_sel_hi:[1,0,1]
	v_add_f32_e32 v94, v132, v133
	v_add_f32_e32 v95, v74, v75
	v_add_f32_e32 v91, v142, v91
	v_add_f32_e32 v88, v88, v90
	v_add_f32_e32 v94, v95, v94
	v_add_f32_e32 v95, v70, v71
	v_add_f32_e32 v143, v76, v77
	v_add_f32_e32 v88, v88, v91
	v_add_f32_e32 v95, v143, v95
	v_add_f32_e32 v88, v88, v94
	v_add_f32_e32 v88, v88, v95
	v_add_f32_e32 v88, v88, v131
	s_nop 1
	v_add_f32_dpp v88, v88, v88 quad_perm:[1,0,3,2] row_mask:0xf bank_mask:0xf bound_ctrl:1
	s_nop 1
	v_add_f32_dpp v88, v88, v88 quad_perm:[2,3,0,1] row_mask:0xf bank_mask:0xf bound_ctrl:1
	s_nop 1
	v_add_f32_dpp v88, v88, v88 row_half_mirror row_mask:0xf bank_mask:0xf bound_ctrl:1
	s_nop 1
	v_add_f32_dpp v88, v88, v88 row_mirror row_mask:0xf bank_mask:0xf bound_ctrl:1
	v_mov_b32_e32 v89, v88
	s_nop 1
	v_permlane16_swap_b32_e32 v88, v89
	v_add_f32_e32 v88, v88, v89
	v_mov_b32_e32 v89, v88
	s_nop 1
	v_permlane32_swap_b32_e32 v88, v89
	v_add_f32_e32 v88, v88, v89
	v_fmac_f32_e32 v69, 0xba000000, v88
	v_fmac_f32_e32 v67, 0xba000000, v88
	v_fmac_f32_e32 v79, 0xba000000, v88
	v_fmac_f32_e32 v73, 0xba000000, v88
	v_fmamk_f32 v68, v88, 0xba000000, v68
	v_fmamk_f32 v66, v88, 0xba000000, v66
	v_fmamk_f32 v78, v88, 0xba000000, v78
	v_fmamk_f32 v72, v88, 0xba000000, v72
	v_fmamk_f32 v84, v88, 0xba000000, v84
	v_fmac_f32_e32 v85, 0xba000000, v88
	v_fmamk_f32 v80, v88, 0xba000000, v80
	v_fmac_f32_e32 v81, 0xba000000, v88
	v_fmamk_f32 v92, v88, 0xba000000, v92
	v_fmac_f32_e32 v93, 0xba000000, v88
	v_fmamk_f32 v82, v88, 0xba000000, v82
	v_fmac_f32_e32 v83, 0xba000000, v88
	v_fmamk_f32 v64, v88, 0xba000000, v64
	v_fmac_f32_e32 v65, 0xba000000, v88
	v_fmamk_f32 v86, v88, 0xba000000, v86
	v_fmac_f32_e32 v87, 0xba000000, v88
	v_fmamk_f32 v132, v88, 0xba000000, v132
	v_fmac_f32_e32 v133, 0xba000000, v88
	v_fmamk_f32 v74, v88, 0xba000000, v74
	v_fmac_f32_e32 v75, 0xba000000, v88
	v_fmamk_f32 v70, v88, 0xba000000, v70
	v_fmac_f32_e32 v71, 0xba000000, v88
	v_fmamk_f32 v76, v88, 0xba000000, v76
	v_fmac_f32_e32 v77, 0xba000000, v88
	v_fmamk_f32 v140, v88, 0xba000000, v140
	v_fmac_f32_e32 v141, 0xba000000, v88
	v_fmamk_f32 v138, v88, 0xba000000, v138
	v_fmac_f32_e32 v139, 0xba000000, v88
	v_mul_f32_e32 v88, v67, v67
	v_mul_f32_e32 v89, v69, v69
	v_mul_f32_e32 v90, v73, v73
	v_mul_f32_e32 v91, v79, v79
	v_mul_f32_e32 v94, v81, v81
	v_mul_f32_e32 v95, v85, v85
	v_fmac_f32_e32 v88, v66, v66
	v_fmac_f32_e32 v89, v68, v68
	v_fmac_f32_e32 v90, v72, v72
	v_fmac_f32_e32 v91, v78, v78
	v_mul_f32_e32 v131, v83, v83
	v_mul_f32_e32 v134, v93, v93
	v_fmac_f32_e32 v94, v80, v80
	v_fmac_f32_e32 v95, v84, v84
	v_add_f32_e32 v88, v88, v89
	v_add_f32_e32 v89, v90, v91
	v_mul_f32_e32 v135, v87, v87
	v_mul_f32_e32 v136, v65, v65
	v_fmac_f32_e32 v131, v82, v82
	v_fmac_f32_e32 v134, v92, v92
	v_add_f32_e32 v90, v94, v95
	v_add_f32_e32 v88, v88, v89
	v_mul_f32_e32 v137, v75, v75
	v_mul_f32_e32 v142, v133, v133
	v_fmac_f32_e32 v135, v86, v86
	v_fmac_f32_e32 v136, v64, v64
	v_add_f32_e32 v91, v131, v134
	v_add_f32_e32 v88, v88, v90
	v_mul_f32_e32 v143, v77, v77
	v_mul_f32_e32 v144, v71, v71
	v_fmac_f32_e32 v137, v74, v74
	v_fmac_f32_e32 v142, v132, v132
	v_add_f32_e32 v94, v135, v136
	v_add_f32_e32 v88, v88, v91
	v_mul_f32_e32 v145, v139, v139
	v_mul_f32_e32 v146, v141, v141
	v_fmac_f32_e32 v143, v76, v76
	v_fmac_f32_e32 v144, v70, v70
	v_add_f32_e32 v95, v137, v142
	v_add_f32_e32 v88, v88, v94
	v_fmac_f32_e32 v145, v138, v138
	v_fmac_f32_e32 v146, v140, v140
	v_add_f32_e32 v131, v143, v144
	v_add_f32_e32 v88, v88, v95
	v_add_f32_e32 v134, v145, v146
	v_add_f32_e32 v88, v88, v131
	v_add_f32_e32 v88, v88, v134
	s_nop 1
	v_add_f32_dpp v88, v88, v88 quad_perm:[1,0,3,2] row_mask:0xf bank_mask:0xf bound_ctrl:1
	s_nop 1
	v_add_f32_dpp v88, v88, v88 quad_perm:[2,3,0,1] row_mask:0xf bank_mask:0xf bound_ctrl:1
	s_nop 1
	v_add_f32_dpp v88, v88, v88 row_half_mirror row_mask:0xf bank_mask:0xf bound_ctrl:1
	s_nop 1
	v_add_f32_dpp v88, v88, v88 row_mirror row_mask:0xf bank_mask:0xf bound_ctrl:1
	v_mov_b32_e32 v89, v88
	s_nop 1
	v_permlane16_swap_b32_e32 v88, v89
	v_add_f32_e32 v88, v88, v89
	v_mov_b32_e32 v89, v88
	s_nop 1
	v_permlane32_swap_b32_e32 v88, v89
	v_add_f32_e32 v88, v88, v89
	v_fmamk_f32 v88, v88, 0x3a000000, v127
	v_mul_f32_e32 v89, 0x4f800000, v88
	v_cmp_gt_f32_e32 vcc, s20, v88
	s_nop 1
	v_cndmask_b32_e32 v88, v88, v89, vcc
	v_sqrt_f32_e32 v89, v88
	s_nop 0
	v_add_u32_e32 v90, -1, v89
	v_add_u32_e32 v91, 1, v89
	v_fma_f32 v94, -v90, v89, v88
	v_fma_f32 v95, -v91, v89, v88
	v_cmp_ge_f32_e64 s[2:3], 0, v94
	s_nop 1
	v_cndmask_b32_e64 v89, v89, v90, s[2:3]
	v_cmp_lt_f32_e64 s[2:3], 0, v95
	s_nop 1
	v_cndmask_b32_e64 v89, v89, v91, s[2:3]
	v_mul_f32_e32 v90, 0x37800000, v89
	v_cndmask_b32_e32 v89, v89, v90, vcc
	v_cmp_class_f32_e32 vcc, v88, v128
	s_nop 1
	v_cndmask_b32_e32 v88, v89, v88, vcc
	v_div_scale_f32 v89, s[2:3], v88, v88, 1.0
	v_rcp_f32_e32 v91, v89
	v_div_scale_f32 v90, vcc, 1.0, v88, 1.0
	v_fma_f32 v94, -v89, v91, 1.0
	v_fmac_f32_e32 v91, v94, v91
	v_mul_f32_e32 v94, v90, v91
	v_fma_f32 v95, -v89, v94, v90
	v_fmac_f32_e32 v94, v95, v91
	v_fma_f32 v89, -v89, v94, v90
	v_div_fmas_f32 v89, v89, v91, v94
	v_div_fixup_f32 v88, v89, v88, 1.0
	v_pk_mul_f32 v[66:67], v[88:89], v[66:67] op_sel_hi:[0,1]
	v_pk_mul_f32 v[68:69], v[88:89], v[68:69] op_sel_hi:[0,1]
	v_pk_mul_f32 v[72:73], v[88:89], v[72:73] op_sel_hi:[0,1]
	v_pk_mul_f32 v[78:79], v[88:89], v[78:79] op_sel_hi:[0,1]
	v_pk_mul_f32 v[80:81], v[88:89], v[80:81] op_sel_hi:[0,1]
	v_pk_mul_f32 v[84:85], v[88:89], v[84:85] op_sel_hi:[0,1]
	v_pk_mul_f32 v[82:83], v[88:89], v[82:83] op_sel_hi:[0,1]
	v_pk_mul_f32 v[90:91], v[88:89], v[92:93] op_sel_hi:[0,1]
	v_pk_mul_f32 v[86:87], v[88:89], v[86:87] op_sel_hi:[0,1]
	v_pk_mul_f32 v[64:65], v[88:89], v[64:65] op_sel_hi:[0,1]
	v_pk_mul_f32 v[74:75], v[88:89], v[74:75] op_sel_hi:[0,1]
	v_pk_mul_f32 v[92:93], v[88:89], v[132:133] op_sel_hi:[0,1]
	v_pk_mul_f32 v[76:77], v[88:89], v[76:77] op_sel_hi:[0,1]
	v_pk_mul_f32 v[70:71], v[88:89], v[70:71] op_sel_hi:[0,1]
	v_pk_mul_f32 v[94:95], v[88:89], v[140:141] op_sel_hi:[0,1]
	v_pk_mul_f32 v[88:89], v[88:89], v[138:139] op_sel_hi:[0,1]
	s_waitcnt lgkmcnt(13)
	v_pk_fma_f32 v[18:19], v[68:69], v[18:19], v[50:51]
	v_pk_fma_f32 v[16:17], v[66:67], v[16:17], v[48:49]
	s_mov_b64 vcc, s[0:1]
	s_waitcnt lgkmcnt(12)
	v_pk_fma_f32 v[2:3], v[78:79], v[2:3], v[34:35]
	v_pk_fma_f32 v[0:1], v[72:73], v[0:1], v[32:33]
	s_waitcnt lgkmcnt(9)
	v_pk_fma_f32 v[22:23], v[84:85], v[22:23], v[54:55]
	v_pk_fma_f32 v[20:21], v[80:81], v[20:21], v[52:53]
	s_waitcnt lgkmcnt(8)
	v_pk_fma_f32 v[6:7], v[90:91], v[6:7], v[38:39]
	v_pk_fma_f32 v[4:5], v[82:83], v[4:5], v[36:37]
	s_waitcnt lgkmcnt(5)
	v_pk_fma_f32 v[26:27], v[64:65], v[26:27], v[58:59]
	v_pk_fma_f32 v[24:25], v[86:87], v[24:25], v[56:57]
	s_waitcnt lgkmcnt(4)
	v_pk_fma_f32 v[10:11], v[92:93], v[10:11], v[42:43]
	v_pk_fma_f32 v[8:9], v[74:75], v[8:9], v[40:41]
	s_waitcnt lgkmcnt(1)
	v_pk_fma_f32 v[30:31], v[70:71], v[30:31], v[62:63]
	v_pk_fma_f32 v[28:29], v[76:77], v[28:29], v[60:61]
	s_waitcnt lgkmcnt(0)
	v_pk_fma_f32 v[12:13], v[88:89], v[12:13], v[44:45]
	v_pk_fma_f32 v[14:15], v[94:95], v[14:15], v[46:47]
	global_store_dwordx4 v[116:117], v[16:19], off sc0 sc1
	global_store_dwordx4 v[116:117], v[0:3], off offset:1024 sc0 sc1
	global_store_dwordx4 v[116:117], v[20:23], off offset:2048 sc0 sc1
	global_store_dwordx4 v[116:117], v[4:7], off offset:3072 sc0 sc1
	global_store_dwordx4 v[118:119], v[24:27], off sc0 sc1
	global_store_dwordx4 v[120:121], v[8:11], off sc0 sc1
	global_store_dwordx4 v[122:123], v[28:31], off sc0 sc1
	global_store_dwordx4 v[124:125], v[12:15], off sc0 sc1
	s_cbranch_vccnz .LBB0_1205
